# moe_stagger step 75 (8 groups x ~2.0us)
# baseline (speedup 1.0000x reference)
.Lstg_loop:
	s_sleep 75
	s_add_i32 s98, s98, -1
	s_cmp_lg_u32 s98, 0
	s_cbranch_scc1 .Lstg_loop
